# v32 + scan step reads the decay factors before the K fragments and applies the state decay under the K reads (counted wait)
# baseline (speedup 1.0000x reference)
.LBB0_557:
	v_add_u32_e32 v132, s6, v131
	ds_read_b128 v[154:157], v132 offset:45056
	ds_read_b128 v[158:161], v132 offset:45088
	ds_read_b128 v[162:165], v132 offset:45120
	ds_read_b128 v[166:169], v132 offset:45152
	ds_read_b128 v[170:173], v132 offset:45184
	ds_read_b128 v[174:177], v132 offset:45216
	ds_read_b128 v[178:181], v132 offset:45248
	ds_read_b128 v[182:185], v132 offset:45280
	ds_read_b128 v[186:189], v132 offset:45312
	ds_read_b128 v[190:193], v132 offset:45344
	ds_read_b128 v[198:201], v132 offset:45376
	ds_read_b128 v[202:205], v132 offset:45408
	ds_read_b128 v[206:209], v132 offset:45440
	ds_read_b128 v[210:213], v132 offset:45472
	ds_read_b128 v[214:217], v132 offset:45504
	ds_read_b128 v[218:221], v132 offset:45536
	ds_read_b128 v[138:141], v136 offset:16384
	ds_read_b128 v[114:117], v136 offset:17408
	ds_read_b128 v[82:85], v136 offset:18432
	ds_read_b128 v[70:73], v136 offset:19456
	ds_read_b128 v[142:145], v136 offset:20480
	ds_read_b128 v[118:121], v136 offset:21504
	ds_read_b128 v[86:89], v136 offset:22528
	ds_read_b128 v[74:77], v136 offset:23552
	ds_read_b128 v[146:149], v136 offset:24576
	ds_read_b128 v[122:125], v136 offset:25600
	ds_read_b128 v[90:93], v136 offset:26624
	ds_read_b128 v[78:81], v136 offset:27648
	ds_read_b128 v[150:153], v136 offset:28672
	ds_read_b128 v[126:129], v136 offset:29696
	ds_read_b128 v[94:97], v136 offset:30720
	ds_read_b128 v[66:69], v136 offset:31744
	s_add_i32 s10, s10, 1
	s_waitcnt lgkmcnt(15)
	v_pk_mul_f32 v[2:3], v[2:3], v[154:155]
	v_pk_mul_f32 v[4:5], v[4:5], v[156:157]
	v_pk_mul_f32 v[6:7], v[6:7], v[158:159]
	v_pk_mul_f32 v[8:9], v[8:9], v[160:161]
	v_pk_mul_f32 v[10:11], v[10:11], v[162:163]
	v_pk_mul_f32 v[12:13], v[12:13], v[164:165]
	v_pk_mul_f32 v[14:15], v[14:15], v[166:167]
	v_pk_mul_f32 v[16:17], v[16:17], v[168:169]
	v_pk_mul_f32 v[18:19], v[18:19], v[170:171]
	v_pk_mul_f32 v[20:21], v[20:21], v[172:173]
	v_pk_mul_f32 v[22:23], v[22:23], v[174:175]
	v_pk_mul_f32 v[24:25], v[24:25], v[176:177]
	v_pk_mul_f32 v[26:27], v[26:27], v[178:179]
	v_pk_mul_f32 v[28:29], v[28:29], v[180:181]
	v_pk_mul_f32 v[30:31], v[30:31], v[182:183]
	v_pk_mul_f32 v[32:33], v[32:33], v[184:185]
	v_pk_mul_f32 v[34:35], v[34:35], v[186:187]
	v_pk_mul_f32 v[36:37], v[36:37], v[188:189]
	v_pk_mul_f32 v[38:39], v[38:39], v[190:191]
	v_pk_mul_f32 v[40:41], v[40:41], v[192:193]
	v_pk_mul_f32 v[42:43], v[42:43], v[198:199]
	v_pk_mul_f32 v[44:45], v[44:45], v[200:201]
	v_pk_mul_f32 v[46:47], v[46:47], v[202:203]
	v_pk_mul_f32 v[48:49], v[48:49], v[204:205]
	v_pk_mul_f32 v[50:51], v[50:51], v[206:207]
	v_pk_mul_f32 v[52:53], v[52:53], v[208:209]
	v_pk_mul_f32 v[54:55], v[54:55], v[210:211]
	v_pk_mul_f32 v[56:57], v[56:57], v[212:213]
	v_pk_mul_f32 v[58:59], v[58:59], v[214:215]
	v_pk_mul_f32 v[60:61], v[60:61], v[216:217]
	v_pk_mul_f32 v[62:63], v[62:63], v[218:219]
	v_pk_mul_f32 v[64:65], v[64:65], v[220:221]
	s_waitcnt lgkmcnt(0)
	v_mov_b32_e32 v132, s17
	v_mov_b32_e32 v136, s10
	ds_write_b32 v132, v136
	v_mfma_f32_32x32x16_bf16 v[2:17], v[138:141], v[110:113], v[2:17]
	s_cmpk_eq_i32 s10, 0x44
	v_mfma_f32_32x32x16_bf16 v[18:33], v[142:145], v[110:113], v[18:33]
	v_mfma_f32_32x32x16_bf16 v[34:49], v[146:149], v[110:113], v[34:49]
	v_mfma_f32_32x32x16_bf16 v[50:65], v[150:153], v[110:113], v[50:65]
	v_mfma_f32_32x32x16_bf16 v[2:17], v[114:117], v[106:109], v[2:17]
	v_mfma_f32_32x32x16_bf16 v[18:33], v[118:121], v[106:109], v[18:33]
	v_mfma_f32_32x32x16_bf16 v[34:49], v[122:125], v[106:109], v[34:49]
	v_mfma_f32_32x32x16_bf16 v[50:65], v[126:129], v[106:109], v[50:65]
	v_mfma_f32_32x32x16_bf16 v[2:17], v[82:85], v[102:105], v[2:17]
	v_mfma_f32_32x32x16_bf16 v[18:33], v[86:89], v[102:105], v[18:33]
	v_mfma_f32_32x32x16_bf16 v[34:49], v[90:93], v[102:105], v[34:49]
	v_mfma_f32_32x32x16_bf16 v[50:65], v[94:97], v[102:105], v[50:65]
	v_mfma_f32_32x32x16_bf16 v[2:17], v[70:73], v[98:101], v[2:17]
	v_mfma_f32_32x32x16_bf16 v[18:33], v[74:77], v[98:101], v[18:33]
	v_mfma_f32_32x32x16_bf16 v[34:49], v[78:81], v[98:101], v[34:49]
	v_mfma_f32_32x32x16_bf16 v[50:65], v[66:69], v[98:101], v[50:65]
	s_cbranch_scc1 .LBB0_573
